# first mod-norm row phase: each wave touches its next input row (one dword per 64 B) right after issuing the current row's loads
# baseline (speedup 1.0000x reference)
; __device__ __forceinline__ float wave_sum(float v) {
; #pragma unroll
;     for (int o = 1; o < 64; o <<= 1) v += __shfl_xor(v, o);
;     return v;
; __device__ __forceinline__ void phase_modnorm0(Frame& F) {
;     const int gw = F.vcu * NWAVES + F.wave, NGW = F.G * NWAVES, R = (T0 + NGW - 1) / NGW;
;     const int r0 = gw * R, r1 = (r0 + R < T0) ? r0 + R : T0;
;     int crb = -1; f32x4 A[4], B[4];
;     for (int row = r0; row < r1; ++row) {
.LBB0_187:
	s_cmp_lt_i32 s34, 2
	s_cselect_b64 s[4:5], -1, 0
	s_and_b64 s[0:1], s[4:5], s[0:1]
	s_andn2_b64 vcc, exec, s[0:1]
	s_cbranch_vccnz .LBB0_197
	s_lshl_b32 s1, s67, 3
	s_abs_i32 s3, s1
	v_cvt_f32_u32_e32 v2, s3
	v_mov_b32_e32 v1, v0
	s_lshl_b32 s0, s71, 3
	v_rcp_iflag_f32_e32 v2, v2
	v_readfirstlane_b32 s9, v1
	s_add_i32 s2, s1, 0x87ff
	s_ashr_i32 s9, s9, 6
	v_mul_f32_e32 v2, 0x4f7ffffe, v2
	v_cvt_u32_f32_e32 v2, v2
	s_add_i32 s9, s9, s0
	s_xor_b32 s0, s2, s1
	s_abs_i32 s1, s2
	s_sub_i32 s2, 0, s3
	v_readfirstlane_b32 s10, v2
	s_mul_i32 s2, s2, s10
	s_mul_hi_u32 s2, s10, s2
	s_add_i32 s10, s10, s2
	s_mul_hi_u32 s2, s1, s10
	s_mul_i32 s10, s2, s3
	s_sub_i32 s1, s1, s10
	s_ashr_i32 s0, s0, 31
	s_add_i32 s10, s2, 1
	s_sub_i32 s11, s1, s3
	s_cmp_ge_u32 s1, s3
	s_cselect_b32 s2, s10, s2
	s_cselect_b32 s1, s11, s1
	s_add_i32 s10, s2, 1
	s_cmp_ge_u32 s1, s3
	s_cselect_b32 s1, s10, s2
	s_xor_b32 s1, s1, s0
	s_sub_i32 s1, s1, s0
	s_mul_i32 s0, s1, s9
	s_add_i32 s1, s0, s1
	s_min_i32 s9, s1, 0x8800
	s_cmp_ge_i32 s0, s9
	s_mov_b32 s3, 0
	s_cbranch_scc1 .LBB0_197
	v_and_b32_e32 v34, 63, v1
	v_mbcnt_lo_u32_b32 v1, -1, 0
	v_mbcnt_hi_u32_b32 v2, -1, v1
	v_and_b32_e32 v1, 64, v2
	v_add_u32_e32 v3, 64, v1
	v_xor_b32_e32 v1, 1, v2
	v_cmp_lt_i32_e32 vcc, v1, v3
	v_xor_b32_e32 v4, 2, v2
	s_add_u32 s20, s38, 0x8800000
	v_cndmask_b32_e32 v1, v2, v1, vcc
	v_cmp_lt_i32_e32 vcc, v4, v3
	s_addc_u32 s21, s39, 0
	s_add_u32 s22, s38, 0x100000
	v_cndmask_b32_e32 v4, v2, v4, vcc
	v_lshlrev_b32_e32 v35, 2, v4
	v_xor_b32_e32 v4, 4, v2
	v_cmp_lt_i32_e32 vcc, v4, v3
	s_addc_u32 s23, s39, 0
	s_ashr_i32 s1, s0, 31
	v_cndmask_b32_e32 v4, v2, v4, vcc
	v_lshlrev_b32_e32 v38, 2, v4
	v_xor_b32_e32 v4, 8, v2
	v_cmp_lt_i32_e32 vcc, v4, v3
	s_mov_b32 s47, -1
	v_lshlrev_b32_e32 v1, 2, v1
	v_cndmask_b32_e32 v4, v2, v4, vcc
	v_lshlrev_b32_e32 v39, 2, v4
	v_xor_b32_e32 v4, 16, v2
	v_cmp_lt_i32_e32 vcc, v4, v3
	v_mov_b32_e32 v37, 0
	s_lshl_b64 s[10:11], s[0:1], 12
	v_cndmask_b32_e32 v4, v2, v4, vcc
	v_lshlrev_b32_e32 v40, 2, v4
	v_xor_b32_e32 v4, 32, v2
	v_cmp_lt_i32_e32 vcc, v4, v3
	s_movk_i32 s40, 0x7fff
	s_add_i32 s41, 0, 0x20230
	v_cndmask_b32_e32 v2, v2, v4, vcc
	v_lshlrev_b32_e32 v41, 2, v2
	s_mov_b64 s[12:13], 0x1000
	s_movk_i32 s42, 0x1000
	s_add_i32 s43, 0, 0x20210
	s_add_i32 s44, 0, 0x20200
	v_mov_b32_e32 v42, 0x358637bd
	s_mov_b32 s45, 0x800000
	s_mov_b32 s46, 0xffff0000
	v_lshlrev_b32_e32 v36, 4, v34
	v_lshlrev_b32_e32 v77, 6, v34
	s_branch .LBB0_191
; template <class T> __device__ __forceinline__ T* wsp(const Frame& F, size_t off) { return (T*)(F.ws + off); }
; __device__ __forceinline__ const float* modp(const Frame& F, int layer, int rb, int j) { return wsp<const float>(F, WS_MOD) + ((size_t)(layer * 9 + rb) * 6 + j) * 1024; }
; __device__ __forceinline__ void ldvec(const float* p, int lane, f32x4 (&v)[4]) { ldrow_f32(p, lane, v); }
; #pragma unroll
;     for (int j = 0; j < 4; ++j) s += (v[j].x * v[j].x + v[j].y * v[j].y) + (v[j].z * v[j].z + v[j].w * v[j].w);
;     return rsqrtf(wave_sum(s) * (1.f / DM) + EPSN); }
; __device__ __forceinline__ void phase_modnorm0(Frame& F) {
;     ...
;     for (int row = r0; row < r1; ++row) {
;         const int rb = rowbatch(row);
;         if (rb != crb) { crb = rb; f32x4 g[4], sc[4]; ldvec(inp(F, I_NORMG), F.lane, g); ldvec(modp(F, 0, rb, 1), F.lane, sc); ldvec(modp(F, 0, rb, 0), F.lane, B);
; #pragma unroll
;             for (int j = 0; j < 4; ++j) A[j] = g[j] * (sc[j] + 1.f); }
;         const float* xr = row < TL ? inp(F, I_X) + (size_t)row * DM : inp(F, I_CTX) + (size_t)(row - TL) * DM;
;         f32x4 v[4], o[4]; ldrow_f32_nt(xr, F.lane, v); const float rs = rstd_of(v);
; #pragma unroll
;         for (int j = 0; j < 4; ++j) o[j] = v[j] * rs * A[j] + B[j];
;         strow_bf16(wsp<bf16>(F, WS_HX) + (size_t)row * DM, F.lane, o);
;     }
.LBB0_190:
	global_load_dwordx4 v[44:47], v36, s[16:17] nt
	global_load_dwordx4 v[48:51], v36, s[16:17] offset:1024 nt
	global_load_dwordx4 v[52:55], v36, s[16:17] offset:3072 nt
	global_load_dwordx4 v[56:59], v36, s[16:17] offset:2048 nt
	s_add_i32 s98, s0, 1
	s_cmp_lt_i32 s98, s9
	s_cselect_b32 s99, 0x1000, 0
	s_cmp_lg_u32 s98, 0x8000
	s_cselect_b32 s99, s99, 0
	s_add_u32 s100, s16, s99
	s_addc_u32 s101, s17, 0
	global_load_dword v76, v77, s[100:101]
	s_lshl_b64 s[14:15], s[14:15], 11
	s_add_u32 s14, s20, s14
	s_addc_u32 s15, s21, s15
	s_add_u32 s0, s0, 1
	s_addc_u32 s1, s1, 0
	s_add_u32 s10, s10, 0x1000
	s_addc_u32 s11, s11, 0
	s_cmp_lt_i32 s0, s9
	s_waitcnt vmcnt(1)
	v_pk_mul_f32 v[60:61], v[46:47], v[46:47]
	v_pk_mul_f32 v[62:63], v[44:45], v[44:45]
	v_pk_mul_f32 v[64:65], v[50:51], v[50:51]
	v_pk_mul_f32 v[66:67], v[48:49], v[48:49]
	v_pk_mov_b32 v[72:73], v[62:63], v[60:61] op_sel:[1,0]
	v_mov_b32_e32 v63, v61
	v_pk_mov_b32 v[60:61], v[66:67], v[64:65] op_sel:[1,0]
	v_mov_b32_e32 v67, v65
	v_mul_f32_e32 v71, v53, v53
	v_mul_f32_e32 v68, v57, v57
	v_mul_f32_e32 v70, v59, v59
	v_pk_add_f32 v[62:63], v[72:73], v[62:63]
	v_pk_add_f32 v[60:61], v[60:61], v[66:67]
	v_mul_f32_e32 v43, v52, v52
	v_mul_f32_e32 v74, v54, v54
	v_mul_f32_e32 v75, v55, v55
	v_pk_fma_f32 v[64:65], v[56:57], v[56:57], v[68:69] op_sel_hi:[1,1,0]
	v_pk_fma_f32 v[68:69], v[58:59], v[58:59], v[70:71] op_sel_hi:[1,1,0]
	v_pk_add_f32 v[62:63], v[62:63], v[62:63] op_sel:[0,1] op_sel_hi:[1,0]
	v_pk_add_f32 v[60:61], v[60:61], v[60:61] op_sel:[0,1] op_sel_hi:[1,0]
	v_mov_b32_e32 v65, v74
	v_mov_b32_e32 v69, v75
	v_mov_b32_e32 v63, v43
	v_mov_b32_e32 v61, v71
	v_pk_add_f32 v[64:65], v[64:65], v[68:69]
	v_pk_add_f32 v[60:61], v[62:63], v[60:61]
	s_nop 0
	v_pk_add_f32 v[60:61], v[60:61], v[64:65]
	s_nop 0
	v_add_f32_e32 v43, v60, v61
	ds_bpermute_b32 v60, v1, v43
	v_lshlrev_b32_e32 v61, 3, v34
	s_waitcnt lgkmcnt(0)
	v_add_f32_e32 v43, v43, v60
	ds_bpermute_b32 v60, v35, v43
	s_waitcnt lgkmcnt(0)
	v_add_f32_e32 v43, v43, v60
	ds_bpermute_b32 v60, v38, v43
	s_waitcnt lgkmcnt(0)
	v_add_f32_e32 v43, v43, v60
	ds_bpermute_b32 v60, v39, v43
	s_waitcnt lgkmcnt(0)
	v_add_f32_e32 v43, v43, v60
	ds_bpermute_b32 v60, v40, v43
	s_waitcnt lgkmcnt(0)
	v_add_f32_e32 v43, v43, v60
	ds_bpermute_b32 v60, v41, v43
	s_waitcnt lgkmcnt(0)
	v_add_f32_e32 v43, v43, v60
	v_fmamk_f32 v43, v43, 0x3a800000, v42
	v_mul_f32_e32 v60, 0x4b800000, v43
	v_cmp_gt_f32_e32 vcc, s45, v43
	s_nop 1
	v_cndmask_b32_e32 v43, v43, v60, vcc
	v_rsq_f32_e32 v43, v43
	s_nop 0
	v_mul_f32_e32 v60, 0x45800000, v43
	v_cndmask_b32_e32 v60, v43, v60, vcc
	v_pk_mul_f32 v[44:45], v[44:45], v[60:61] op_sel_hi:[1,0]
	v_pk_mul_f32 v[46:47], v[46:47], v[60:61] op_sel_hi:[1,0]
	v_pk_mul_f32 v[48:49], v[48:49], v[60:61] op_sel_hi:[1,0]
	v_pk_mul_f32 v[50:51], v[50:51], v[60:61] op_sel_hi:[1,0]
	v_pk_mul_f32 v[56:57], v[56:57], v[60:61] op_sel_hi:[1,0]
	v_pk_mul_f32 v[58:59], v[58:59], v[60:61] op_sel_hi:[1,0]
	v_pk_mul_f32 v[52:53], v[52:53], v[60:61] op_sel_hi:[1,0]
	v_pk_mul_f32 v[54:55], v[54:55], v[60:61] op_sel_hi:[1,0]
	v_pk_fma_f32 v[46:47], v[20:21], v[46:47], v[16:17]
	v_pk_fma_f32 v[44:45], v[18:19], v[44:45], v[14:15]
	v_pk_fma_f32 v[50:51], v[24:25], v[50:51], v[12:13]
	v_pk_fma_f32 v[48:49], v[22:23], v[48:49], v[10:11]
	v_pk_fma_f32 v[58:59], v[28:29], v[58:59], v[8:9]
	v_pk_fma_f32 v[56:57], v[26:27], v[56:57], v[6:7]
	v_pk_fma_f32 v[54:55], v[32:33], v[54:55], v[4:5]
	v_pk_fma_f32 v[52:53], v[30:31], v[52:53], v[2:3]
	v_bfe_u32 v43, v44, 16, 1
	v_bfe_u32 v60, v45, 16, 1
	v_bfe_u32 v62, v46, 16, 1
	v_bfe_u32 v63, v47, 16, 1
	v_bfe_u32 v64, v48, 16, 1
	v_bfe_u32 v65, v49, 16, 1
	v_bfe_u32 v66, v50, 16, 1
	v_bfe_u32 v67, v51, 16, 1
	v_bfe_u32 v68, v56, 16, 1
	v_bfe_u32 v69, v57, 16, 1
	v_bfe_u32 v70, v58, 16, 1
	v_bfe_u32 v72, v52, 16, 1
	v_bfe_u32 v74, v54, 16, 1
	v_add3_u32 v43, v44, v43, s40
	v_add3_u32 v44, v45, v60, s40
	v_add3_u32 v45, v46, v62, s40
	v_bfe_u32 v71, v59, 16, 1
	v_bfe_u32 v73, v53, 16, 1
	v_bfe_u32 v75, v55, 16, 1
	v_add3_u32 v46, v47, v63, s40
	v_add3_u32 v47, v48, v64, s40
	v_add3_u32 v48, v49, v65, s40
	v_add3_u32 v49, v50, v66, s40
	v_add3_u32 v50, v51, v67, s40
	v_add3_u32 v51, v56, v68, s40
	v_add3_u32 v56, v57, v69, s40
	v_add3_u32 v57, v58, v70, s40
	v_add3_u32 v52, v52, v72, s40
	v_add3_u32 v54, v54, v74, s40
	v_lshrrev_b32_e32 v43, 16, v43
	v_lshrrev_b32_e32 v45, 16, v45
	v_add3_u32 v58, v59, v71, s40
	v_add3_u32 v53, v53, v73, s40
	v_add3_u32 v55, v55, v75, s40
	v_lshrrev_b32_e32 v47, 16, v47
	v_lshrrev_b32_e32 v49, 16, v49
	v_lshrrev_b32_e32 v51, 16, v51
	v_lshrrev_b32_e32 v57, 16, v57
	v_lshrrev_b32_e32 v52, 16, v52
	v_lshrrev_b32_e32 v54, 16, v54
	v_and_or_b32 v44, v44, s46, v43
	v_and_or_b32 v45, v46, s46, v45
	v_and_or_b32 v46, v48, s46, v47
	v_and_or_b32 v47, v50, s46, v49
	v_and_or_b32 v48, v56, s46, v51
	v_and_or_b32 v49, v58, s46, v57
	v_and_or_b32 v50, v53, s46, v52
	v_and_or_b32 v51, v55, s46, v54
	global_store_dwordx2 v61, v[44:45], s[14:15]
	global_store_dwordx2 v61, v[46:47], s[14:15] offset:512
	global_store_dwordx2 v61, v[48:49], s[14:15] offset:1024
	global_store_dwordx2 v61, v[50:51], s[14:15] offset:1536
	s_cbranch_scc0 .LBB0_197
